# in-projection epilogue: dead constant moves of the non-rotary path removed
# speedup vs baseline: 1.0117x; 1.0001x over previous
.LBB0_191:
.LBB0_192:
	v_pk_mul_f32 v[22:23], v[160:161], s[18:19] op_sel_hi:[1,0]
	v_pk_mul_f32 v[26:27], v[158:159], s[18:19] op_sel_hi:[1,0]
	v_pk_mul_f32 v[24:25], v[156:157], s[18:19] op_sel_hi:[1,0]
	s_and_b64 vcc, exec, s[6:7]
	v_pk_mul_f32 v[28:29], v[154:155], s[18:19] op_sel_hi:[1,0]
	s_cbranch_vccnz .LBB0_194
	v_and_b32_e32 v19, 64, v195
	v_xor_b32_e32 v0, 32, v195
	v_add_u32_e32 v19, 64, v19
	v_cmp_lt_i32_e32 vcc, v0, v19
	v_mov_b32_e32 v158, v23
	s_waitcnt vmcnt(0)
	v_mov_b32_e32 v159, v13
	v_cndmask_b32_e32 v0, v195, v0, vcc
	v_lshlrev_b32_e32 v0, 2, v0
	ds_bpermute_b32 v19, v0, v22
	ds_bpermute_b32 v33, v0, v24
	ds_bpermute_b32 v20, v0, v26
	ds_bpermute_b32 v21, v0, v27
	ds_bpermute_b32 v30, v0, v28
	s_waitcnt lgkmcnt(4)
	v_mul_f32_e32 v19, v170, v19
	v_mul_f32_e32 v32, v12, v19
	ds_bpermute_b32 v19, v0, v23
	ds_bpermute_b32 v31, v0, v29
	ds_bpermute_b32 v0, v0, v25
	v_mov_b32_e32 v156, v17
	s_waitcnt lgkmcnt(6)
	v_mul_f32_e32 v33, v170, v33
	s_waitcnt lgkmcnt(2)
	v_mul_f32_e32 v157, v170, v19
	v_pk_mul_f32 v[156:157], v[158:159], v[156:157]
	v_pk_mul_f32 v[26:27], v[26:27], v[14:15]
	v_pk_mul_f32 v[20:21], v[170:171], v[20:21]
	v_mul_f32_e32 v22, v22, v16
	v_mul_f32_e32 v154, v8, v33
	v_mov_b32_e32 v23, v156
	v_mov_b32_e32 v33, v157
	v_pk_fma_f32 v[26:27], v[10:11], v[20:21], v[26:27]
	v_pk_add_f32 v[22:23], v[22:23], v[32:33]
	s_waitcnt lgkmcnt(0)
	v_mul_f32_e32 v21, v170, v0
	v_mov_b32_e32 v32, v25
	v_mov_b32_e32 v33, v9
	v_mov_b32_e32 v20, v5
	v_pk_mul_f32 v[20:21], v[32:33], v[20:21]
	v_pk_mul_f32 v[28:29], v[28:29], v[2:3]
	v_pk_mul_f32 v[30:31], v[170:171], v[30:31]
	v_mul_f32_e32 v24, v24, v4
	v_mov_b32_e32 v25, v20
	v_mov_b32_e32 v155, v21
	v_pk_fma_f32 v[28:29], v[6:7], v[30:31], v[28:29]
	v_pk_add_f32 v[24:25], v[24:25], v[154:155]

.LBB0_198:
.LBB0_199:
	v_pk_mul_f32 v[24:25], v[144:145], s[18:19] op_sel_hi:[1,0]
	v_pk_mul_f32 v[28:29], v[142:143], s[18:19] op_sel_hi:[1,0]
	v_pk_mul_f32 v[26:27], v[140:141], s[18:19] op_sel_hi:[1,0]
	s_and_b64 vcc, exec, s[6:7]
	v_pk_mul_f32 v[30:31], v[138:139], s[18:19] op_sel_hi:[1,0]
	s_cbranch_vccnz .LBB0_201
	v_and_b32_e32 v19, 64, v195
	v_xor_b32_e32 v0, 32, v195
	v_add_u32_e32 v19, 64, v19
	v_cmp_lt_i32_e32 vcc, v0, v19
	v_mov_b32_e32 v146, v25
	s_waitcnt vmcnt(1)
	v_mov_b32_e32 v147, v13
	v_cndmask_b32_e32 v0, v195, v0, vcc
	v_lshlrev_b32_e32 v0, 2, v0
	ds_bpermute_b32 v19, v0, v24
	ds_bpermute_b32 v32, v0, v28
	ds_bpermute_b32 v33, v0, v29
	ds_bpermute_b32 v138, v0, v30
	ds_bpermute_b32 v139, v0, v31
	s_waitcnt lgkmcnt(4)
	v_mul_f32_e32 v19, v170, v19
	v_mul_f32_e32 v140, v12, v19
	ds_bpermute_b32 v19, v0, v25
	ds_bpermute_b32 v23, v0, v26
	ds_bpermute_b32 v0, v0, v27
	v_mov_b32_e32 v144, v17
	v_pk_mul_f32 v[28:29], v[28:29], v[14:15]
	s_waitcnt lgkmcnt(2)
	v_mul_f32_e32 v145, v170, v19
	v_pk_mul_f32 v[144:145], v[146:147], v[144:145]
	v_pk_mul_f32 v[32:33], v[170:171], v[32:33]
	v_mul_f32_e32 v24, v24, v16
	v_mov_b32_e32 v25, v144
	v_mov_b32_e32 v141, v145
	v_pk_fma_f32 v[28:29], v[10:11], v[32:33], v[28:29]
	v_pk_add_f32 v[24:25], v[24:25], v[140:141]
	s_waitcnt lgkmcnt(0)
	v_mul_f32_e32 v33, v170, v0
	v_mov_b32_e32 v140, v27
	s_waitcnt vmcnt(0)
	v_mov_b32_e32 v141, v9
	v_mov_b32_e32 v32, v5
	v_mul_f32_e32 v23, v170, v23
	v_pk_mul_f32 v[32:33], v[140:141], v[32:33]
	v_pk_mul_f32 v[30:31], v[30:31], v[2:3]
	v_pk_mul_f32 v[138:139], v[170:171], v[138:139]
	v_mul_f32_e32 v26, v26, v4
	v_mul_f32_e32 v142, v8, v23
	v_mov_b32_e32 v27, v32
	v_mov_b32_e32 v143, v33
	v_pk_fma_f32 v[30:31], v[6:7], v[138:139], v[30:31]
	v_pk_add_f32 v[26:27], v[26:27], v[142:143]

.LBB0_205:
.LBB0_206:
	v_pk_mul_f32 v[24:25], v[128:129], s[18:19] op_sel_hi:[1,0]
	v_pk_mul_f32 v[28:29], v[126:127], s[18:19] op_sel_hi:[1,0]
	v_pk_mul_f32 v[26:27], v[124:125], s[18:19] op_sel_hi:[1,0]
	s_and_b64 vcc, exec, s[6:7]
	v_pk_mul_f32 v[30:31], v[122:123], s[18:19] op_sel_hi:[1,0]
	s_cbranch_vccnz .LBB0_208
	v_and_b32_e32 v19, 64, v195
	v_xor_b32_e32 v0, 32, v195
	v_add_u32_e32 v19, 64, v19
	v_cmp_lt_i32_e32 vcc, v0, v19
	v_mov_b32_e32 v130, v25
	s_waitcnt vmcnt(1)
	v_mov_b32_e32 v131, v13
	v_cndmask_b32_e32 v0, v195, v0, vcc
	v_lshlrev_b32_e32 v0, 2, v0
	ds_bpermute_b32 v19, v0, v24
	ds_bpermute_b32 v32, v0, v28
	ds_bpermute_b32 v33, v0, v29
	ds_bpermute_b32 v122, v0, v30
	ds_bpermute_b32 v123, v0, v31
	s_waitcnt lgkmcnt(4)
	v_mul_f32_e32 v19, v170, v19
	v_mul_f32_e32 v124, v12, v19
	ds_bpermute_b32 v19, v0, v25
	ds_bpermute_b32 v23, v0, v26
	ds_bpermute_b32 v0, v0, v27
	v_mov_b32_e32 v128, v17
	v_pk_mul_f32 v[28:29], v[28:29], v[14:15]
	s_waitcnt lgkmcnt(2)
	v_mul_f32_e32 v129, v170, v19
	v_pk_mul_f32 v[128:129], v[130:131], v[128:129]
	v_pk_mul_f32 v[32:33], v[170:171], v[32:33]
	v_mul_f32_e32 v24, v24, v16
	v_mov_b32_e32 v25, v128
	v_mov_b32_e32 v125, v129
	v_pk_fma_f32 v[28:29], v[10:11], v[32:33], v[28:29]
	v_pk_add_f32 v[24:25], v[24:25], v[124:125]
	s_waitcnt lgkmcnt(0)
	v_mul_f32_e32 v33, v170, v0
	v_mov_b32_e32 v124, v27
	s_waitcnt vmcnt(0)
	v_mov_b32_e32 v125, v9
	v_mov_b32_e32 v32, v5
	v_mul_f32_e32 v23, v170, v23
	v_pk_mul_f32 v[32:33], v[124:125], v[32:33]
	v_pk_mul_f32 v[30:31], v[30:31], v[2:3]
	v_pk_mul_f32 v[122:123], v[170:171], v[122:123]
	v_mul_f32_e32 v26, v26, v4
	v_mul_f32_e32 v126, v8, v23
	v_mov_b32_e32 v27, v32
	v_mov_b32_e32 v127, v33
	v_pk_fma_f32 v[30:31], v[6:7], v[122:123], v[30:31]
	v_pk_add_f32 v[26:27], v[26:27], v[126:127]

.LBB0_212:
.LBB0_213:
	v_pk_mul_f32 v[24:25], v[112:113], s[18:19] op_sel_hi:[1,0]
	v_pk_mul_f32 v[28:29], v[110:111], s[18:19] op_sel_hi:[1,0]
	v_pk_mul_f32 v[26:27], v[108:109], s[18:19] op_sel_hi:[1,0]
	s_and_b64 vcc, exec, s[6:7]
	v_pk_mul_f32 v[30:31], v[106:107], s[18:19] op_sel_hi:[1,0]
	s_cbranch_vccnz .LBB0_215
	v_and_b32_e32 v19, 64, v195
	v_xor_b32_e32 v0, 32, v195
	v_add_u32_e32 v19, 64, v19
	v_cmp_lt_i32_e32 vcc, v0, v19
	v_mov_b32_e32 v114, v25
	s_waitcnt vmcnt(1)
	v_mov_b32_e32 v115, v13
	v_cndmask_b32_e32 v0, v195, v0, vcc
	v_lshlrev_b32_e32 v0, 2, v0
	ds_bpermute_b32 v19, v0, v24
	ds_bpermute_b32 v32, v0, v28
	ds_bpermute_b32 v33, v0, v29
	ds_bpermute_b32 v106, v0, v30
	ds_bpermute_b32 v107, v0, v31
	s_waitcnt lgkmcnt(4)
	v_mul_f32_e32 v19, v170, v19
	v_mul_f32_e32 v108, v12, v19
	ds_bpermute_b32 v19, v0, v25
	ds_bpermute_b32 v23, v0, v26
	ds_bpermute_b32 v0, v0, v27
	v_mov_b32_e32 v112, v17
	v_pk_mul_f32 v[28:29], v[28:29], v[14:15]
	s_waitcnt lgkmcnt(2)
	v_mul_f32_e32 v113, v170, v19
	v_pk_mul_f32 v[112:113], v[114:115], v[112:113]
	v_pk_mul_f32 v[32:33], v[170:171], v[32:33]
	v_mul_f32_e32 v24, v24, v16
	v_mov_b32_e32 v25, v112
	v_mov_b32_e32 v109, v113
	v_pk_fma_f32 v[28:29], v[10:11], v[32:33], v[28:29]
	v_pk_add_f32 v[24:25], v[24:25], v[108:109]
	s_waitcnt lgkmcnt(0)
	v_mul_f32_e32 v33, v170, v0
	v_mov_b32_e32 v108, v27
	s_waitcnt vmcnt(0)
	v_mov_b32_e32 v109, v9
	v_mov_b32_e32 v32, v5
	v_mul_f32_e32 v23, v170, v23
	v_pk_mul_f32 v[32:33], v[108:109], v[32:33]
	v_pk_mul_f32 v[30:31], v[30:31], v[2:3]
	v_pk_mul_f32 v[106:107], v[170:171], v[106:107]
	v_mul_f32_e32 v26, v26, v4
	v_mul_f32_e32 v110, v8, v23
	v_mov_b32_e32 v27, v32
	v_mov_b32_e32 v111, v33
	v_pk_fma_f32 v[30:31], v[6:7], v[106:107], v[30:31]
	v_pk_add_f32 v[26:27], v[26:27], v[110:111]

.LBB0_219:
.LBB0_220:
	v_pk_mul_f32 v[24:25], v[96:97], s[18:19] op_sel_hi:[1,0]
	v_pk_mul_f32 v[28:29], v[94:95], s[18:19] op_sel_hi:[1,0]
	v_pk_mul_f32 v[26:27], v[92:93], s[18:19] op_sel_hi:[1,0]
	s_and_b64 vcc, exec, s[6:7]
	v_pk_mul_f32 v[30:31], v[90:91], s[18:19] op_sel_hi:[1,0]
	s_cbranch_vccnz .LBB0_222
	v_and_b32_e32 v19, 64, v195
	v_xor_b32_e32 v0, 32, v195
	v_add_u32_e32 v19, 64, v19
	v_cmp_lt_i32_e32 vcc, v0, v19
	v_mov_b32_e32 v98, v25
	s_waitcnt vmcnt(1)
	v_mov_b32_e32 v99, v13
	v_cndmask_b32_e32 v0, v195, v0, vcc
	v_lshlrev_b32_e32 v0, 2, v0
	ds_bpermute_b32 v19, v0, v24
	ds_bpermute_b32 v32, v0, v28
	ds_bpermute_b32 v33, v0, v29
	ds_bpermute_b32 v90, v0, v30
	ds_bpermute_b32 v91, v0, v31
	s_waitcnt lgkmcnt(4)
	v_mul_f32_e32 v19, v170, v19
	v_mul_f32_e32 v92, v12, v19
	ds_bpermute_b32 v19, v0, v25
	ds_bpermute_b32 v23, v0, v26
	ds_bpermute_b32 v0, v0, v27
	v_mov_b32_e32 v96, v17
	v_pk_mul_f32 v[28:29], v[28:29], v[14:15]
	s_waitcnt lgkmcnt(2)
	v_mul_f32_e32 v97, v170, v19
	v_pk_mul_f32 v[96:97], v[98:99], v[96:97]
	v_pk_mul_f32 v[32:33], v[170:171], v[32:33]
	v_mul_f32_e32 v24, v24, v16
	v_mov_b32_e32 v25, v96
	v_mov_b32_e32 v93, v97
	v_pk_fma_f32 v[28:29], v[10:11], v[32:33], v[28:29]
	v_pk_add_f32 v[24:25], v[24:25], v[92:93]
	s_waitcnt lgkmcnt(0)
	v_mul_f32_e32 v33, v170, v0
	v_mov_b32_e32 v92, v27
	s_waitcnt vmcnt(0)
	v_mov_b32_e32 v93, v9
	v_mov_b32_e32 v32, v5
	v_mul_f32_e32 v23, v170, v23
	v_pk_mul_f32 v[32:33], v[92:93], v[32:33]
	v_pk_mul_f32 v[30:31], v[30:31], v[2:3]
	v_pk_mul_f32 v[90:91], v[170:171], v[90:91]
	v_mul_f32_e32 v26, v26, v4
	v_mul_f32_e32 v94, v8, v23
	v_mov_b32_e32 v27, v32
	v_mov_b32_e32 v95, v33
	v_pk_fma_f32 v[30:31], v[6:7], v[90:91], v[30:31]
	v_pk_add_f32 v[26:27], v[26:27], v[94:95]

.LBB0_226:
.LBB0_227:
	v_pk_mul_f32 v[24:25], v[80:81], s[18:19] op_sel_hi:[1,0]
	v_pk_mul_f32 v[28:29], v[78:79], s[18:19] op_sel_hi:[1,0]
	v_pk_mul_f32 v[26:27], v[76:77], s[18:19] op_sel_hi:[1,0]
	s_and_b64 vcc, exec, s[6:7]
	v_pk_mul_f32 v[30:31], v[74:75], s[18:19] op_sel_hi:[1,0]
	s_cbranch_vccnz .LBB0_229
	v_and_b32_e32 v19, 64, v195
	v_xor_b32_e32 v0, 32, v195
	v_add_u32_e32 v19, 64, v19
	v_cmp_lt_i32_e32 vcc, v0, v19
	v_mov_b32_e32 v82, v25
	s_waitcnt vmcnt(1)
	v_mov_b32_e32 v83, v13
	v_cndmask_b32_e32 v0, v195, v0, vcc
	v_lshlrev_b32_e32 v0, 2, v0
	ds_bpermute_b32 v19, v0, v24
	ds_bpermute_b32 v32, v0, v28
	ds_bpermute_b32 v33, v0, v29
	ds_bpermute_b32 v74, v0, v30
	ds_bpermute_b32 v75, v0, v31
	s_waitcnt lgkmcnt(4)
	v_mul_f32_e32 v19, v170, v19
	v_mul_f32_e32 v76, v12, v19
	ds_bpermute_b32 v19, v0, v25
	ds_bpermute_b32 v23, v0, v26
	ds_bpermute_b32 v0, v0, v27
	v_mov_b32_e32 v80, v17
	v_pk_mul_f32 v[28:29], v[28:29], v[14:15]
	s_waitcnt lgkmcnt(2)
	v_mul_f32_e32 v81, v170, v19
	v_pk_mul_f32 v[80:81], v[82:83], v[80:81]
	v_pk_mul_f32 v[32:33], v[170:171], v[32:33]
	v_mul_f32_e32 v24, v24, v16
	v_mov_b32_e32 v25, v80
	v_mov_b32_e32 v77, v81
	v_pk_fma_f32 v[28:29], v[10:11], v[32:33], v[28:29]
	v_pk_add_f32 v[24:25], v[24:25], v[76:77]
	s_waitcnt lgkmcnt(0)
	v_mul_f32_e32 v33, v170, v0
	v_mov_b32_e32 v76, v27
	s_waitcnt vmcnt(0)
	v_mov_b32_e32 v77, v9
	v_mov_b32_e32 v32, v5
	v_mul_f32_e32 v23, v170, v23
	v_pk_mul_f32 v[32:33], v[76:77], v[32:33]
	v_pk_mul_f32 v[30:31], v[30:31], v[2:3]
	v_pk_mul_f32 v[74:75], v[170:171], v[74:75]
	v_mul_f32_e32 v26, v26, v4
	v_mul_f32_e32 v78, v8, v23
	v_mov_b32_e32 v27, v32
	v_mov_b32_e32 v79, v33
	v_pk_fma_f32 v[30:31], v[6:7], v[74:75], v[30:31]
	v_pk_add_f32 v[26:27], v[26:27], v[78:79]

.LBB0_233:
.LBB0_234:
	v_pk_mul_f32 v[24:25], v[64:65], s[18:19] op_sel_hi:[1,0]
	v_pk_mul_f32 v[28:29], v[62:63], s[18:19] op_sel_hi:[1,0]
	v_pk_mul_f32 v[26:27], v[60:61], s[18:19] op_sel_hi:[1,0]
	s_and_b64 vcc, exec, s[6:7]
	v_pk_mul_f32 v[30:31], v[58:59], s[18:19] op_sel_hi:[1,0]
	s_cbranch_vccnz .LBB0_236
	v_and_b32_e32 v19, 64, v195
	v_xor_b32_e32 v0, 32, v195
	v_add_u32_e32 v19, 64, v19
	v_cmp_lt_i32_e32 vcc, v0, v19
	v_mov_b32_e32 v66, v25
	s_waitcnt vmcnt(1)
	v_mov_b32_e32 v67, v13
	v_cndmask_b32_e32 v0, v195, v0, vcc
	v_lshlrev_b32_e32 v0, 2, v0
	ds_bpermute_b32 v19, v0, v24
	ds_bpermute_b32 v32, v0, v28
	ds_bpermute_b32 v33, v0, v29
	ds_bpermute_b32 v58, v0, v30
	ds_bpermute_b32 v59, v0, v31
	s_waitcnt lgkmcnt(4)
	v_mul_f32_e32 v19, v170, v19
	v_mul_f32_e32 v60, v12, v19
	ds_bpermute_b32 v19, v0, v25
	ds_bpermute_b32 v23, v0, v26
	ds_bpermute_b32 v0, v0, v27
	v_mov_b32_e32 v64, v17
	v_pk_mul_f32 v[28:29], v[28:29], v[14:15]
	s_waitcnt lgkmcnt(2)
	v_mul_f32_e32 v65, v170, v19
	v_pk_mul_f32 v[64:65], v[66:67], v[64:65]
	v_pk_mul_f32 v[32:33], v[170:171], v[32:33]
	v_mul_f32_e32 v24, v24, v16
	v_mov_b32_e32 v25, v64
	v_mov_b32_e32 v61, v65
	v_pk_fma_f32 v[28:29], v[10:11], v[32:33], v[28:29]
	v_pk_add_f32 v[24:25], v[24:25], v[60:61]
	s_waitcnt lgkmcnt(0)
	v_mul_f32_e32 v33, v170, v0
	v_mov_b32_e32 v60, v27
	s_waitcnt vmcnt(0)
	v_mov_b32_e32 v61, v9
	v_mov_b32_e32 v32, v5
	v_mul_f32_e32 v23, v170, v23
	v_pk_mul_f32 v[32:33], v[60:61], v[32:33]
	v_pk_mul_f32 v[30:31], v[30:31], v[2:3]
	v_pk_mul_f32 v[58:59], v[170:171], v[58:59]
	v_mul_f32_e32 v26, v26, v4
	v_mul_f32_e32 v62, v8, v23
	v_mov_b32_e32 v27, v32
	v_mov_b32_e32 v63, v33
	v_pk_fma_f32 v[30:31], v[6:7], v[58:59], v[30:31]
	v_pk_add_f32 v[26:27], v[26:27], v[62:63]

.LBB0_240:
	s_nop 0
.LBB0_241:
	v_pk_mul_f32 v[22:23], v[48:49], s[18:19] op_sel_hi:[1,0]
	v_pk_mul_f32 v[26:27], v[46:47], s[18:19] op_sel_hi:[1,0]
	v_pk_mul_f32 v[24:25], v[44:45], s[18:19] op_sel_hi:[1,0]
	s_and_b64 vcc, exec, s[6:7]
	v_pk_mul_f32 v[28:29], v[42:43], s[18:19] op_sel_hi:[1,0]
	s_cbranch_vccnz .LBB0_243
	v_and_b32_e32 v19, 64, v195
	v_xor_b32_e32 v0, 32, v195
	v_add_u32_e32 v19, 64, v19
	v_cmp_lt_i32_e32 vcc, v0, v19
	v_mov_b32_e32 v48, v23
	s_waitcnt vmcnt(1)
	v_mov_b32_e32 v49, v13
	v_cndmask_b32_e32 v0, v195, v0, vcc
	v_lshlrev_b32_e32 v0, 2, v0
	ds_bpermute_b32 v19, v0, v22
	ds_bpermute_b32 v43, v0, v24
	ds_bpermute_b32 v30, v0, v26
	ds_bpermute_b32 v31, v0, v27
	ds_bpermute_b32 v32, v0, v28
	s_waitcnt lgkmcnt(4)
	v_mul_f32_e32 v19, v170, v19
	v_mul_f32_e32 v42, v12, v19
	ds_bpermute_b32 v19, v0, v23
	ds_bpermute_b32 v33, v0, v29
	ds_bpermute_b32 v0, v0, v25
	v_mov_b32_e32 v46, v17
	s_waitcnt lgkmcnt(6)
	v_mul_f32_e32 v43, v170, v43
	s_waitcnt lgkmcnt(2)
	v_mul_f32_e32 v47, v170, v19
	v_pk_mul_f32 v[46:47], v[48:49], v[46:47]
	v_pk_mul_f32 v[26:27], v[26:27], v[14:15]
	v_pk_mul_f32 v[30:31], v[170:171], v[30:31]
	v_mul_f32_e32 v22, v22, v16
	s_waitcnt vmcnt(0)
	v_mul_f32_e32 v44, v8, v43
	v_mov_b32_e32 v23, v46
	v_mov_b32_e32 v43, v47
	v_pk_fma_f32 v[26:27], v[10:11], v[30:31], v[26:27]
	v_pk_add_f32 v[22:23], v[22:23], v[42:43]
	s_waitcnt lgkmcnt(0)
	v_mul_f32_e32 v31, v170, v0
	v_mov_b32_e32 v42, v25
	v_mov_b32_e32 v43, v9
	v_mov_b32_e32 v30, v5
	v_pk_mul_f32 v[30:31], v[42:43], v[30:31]
	v_pk_mul_f32 v[28:29], v[28:29], v[2:3]
	v_pk_mul_f32 v[32:33], v[170:171], v[32:33]
	v_mul_f32_e32 v24, v24, v4
	v_mov_b32_e32 v25, v30
	v_mov_b32_e32 v45, v31
	v_pk_fma_f32 v[28:29], v[6:7], v[32:33], v[28:29]
	v_pk_add_f32 v[24:25], v[24:25], v[44:45]
